# Z stores of the input-projection GEMM write-through (sc1), table-hook DMA loads non-temporal (nt); no arithmetic change
# baseline (speedup 1.0000x reference)
; #define PG8_LAS __attribute__((address_space(3)))
; __device__ __forceinline__ void hook_issue(const TblHook& h, int it, int lane, PG8_LAS unsigned char* slot) {
;     const int q = __builtin_amdgcn_readfirstlane(it * h.ngw + h.gwave); const int qq = q < HK_NCHUNK ? q : 0; const bool isu = qq < HK_HALF; const int j = isu ? qq : qq - HK_HALF;
;     const __amdgpu_buffer_rsrc_t r = __builtin_amdgcn_make_buffer_rsrc((void*)(isu ? h.u : h.v), (short)0, 0x7fffffff, 0x00020000);
;     const unsigned so = (unsigned)j * 2048u, l16 = (unsigned)lane * 16u;
;     __builtin_amdgcn_raw_ptr_buffer_load_lds(r, (PG8_LAS void*)slot, 16, l16, so, 0, 0);
;     __builtin_amdgcn_raw_ptr_buffer_load_lds(r, (PG8_LAS void*)(slot + 1024), 16, l16, so + 1024u, 0, 0);
.LBB0_183:
	s_andn2_b64 vcc, exec, s[4:5]
	s_mul_i32 s40, s43, s42
	s_cbranch_vccnz .LBB0_185
	s_add_i32 s4, s40, s12
	s_cmp_lt_i32 s4, 0x40000
	s_cselect_b32 s41, s4, 0
	s_cmp_lt_i32 s41, 0x20000
	s_cselect_b64 s[26:27], -1, 0
	s_and_b64 s[4:5], s[26:27], exec
	s_cselect_b32 s4, s58, s60
	s_cselect_b32 s5, s59, s61
	s_lshl_b32 s41, s41, 11
	s_and_b32 s5, s5, 0xffff
	s_add_i32 s93, s41, 0xf0000000
	s_and_b64 s[26:27], s[26:27], exec
	s_mov_b32 m0, s74
	s_cselect_b32 s26, s41, s93
	buffer_load_dwordx4 v214, s[4:7], s26 offen nt lds
	s_bitset1_b32 s26, 10
	s_mov_b32 m0, s75
	s_nop 0
	buffer_load_dwordx4 v214, s[4:7], s26 offen nt lds
	s_waitcnt vmcnt(10)

; __device__ __forceinline__ unsigned cvt_pk_bf16(float lo, float hi) { unsigned r; asm volatile("v_cvt_pk_bf16_f32 %0, %1, %2" : "=v"(r) : "v"(lo), "v"(hi)); return r; }
; __device__ __forceinline__ float sigm(float x) { return __builtin_amdgcn_rcpf(1.0f + __builtin_amdgcn_exp2f(-1.4426950408889634f * x)); }
;     __device__ __forceinline__ void operator()(const f32x4 (&acc)[2][2][4][2], const Unit& u, int wr, int wc, int fr, int fq) const {
;     ...
;             for (int m = 0; m < 4; ++m) { bf16_t* rowp = Z + (size_t)(row0 + ai * HALF + m * 16) * ZLD + col0;
; #pragma unroll
;                 for (int bj = 0; bj < 2; ++bj) { f32x4 v0 = acc[ai][bj][m][0] * scale + bv[bj][0], v1 = acc[ai][bj][m][1] * scale + bv[bj][1];
;                     if (gate) {
; #pragma unroll
;                         for (int j = 0; j < 4; ++j) { v0[j] = sigm(v0[j]); v1[j] = sigm(v1[j]); } }
;                     u32x4 w; w.x = cvt_pk_bf16(v0[0], v0[1]); w.y = cvt_pk_bf16(v0[2], v0[3]); w.z = cvt_pk_bf16(v1[0], v1[1]); w.w = cvt_pk_bf16(v1[2], v1[3]);
;                     *(u32x4*)(rowp + bj * HALF) = w; } }
.LBB0_212:
	v_cvt_f32_i32_e32 v135, v135
	v_cvt_f32_i32_e32 v134, v134
	v_cvt_f32_i32_e32 v137, v137
	v_cvt_f32_i32_e32 v136, v136
	v_cvt_f32_i32_e32 v153, v131
	v_cvt_f32_i32_e32 v152, v130
	v_cvt_f32_i32_e32 v155, v133
	v_cvt_f32_i32_e32 v154, v132
	v_lshl_add_u32 v150, s86, 8, v213
	v_mov_b64_e32 v[138:139], s[54:55]
	v_ashrrev_i32_e32 v147, 31, v146
	v_mad_i64_i32 v[138:139], s[26:27], v150, s72, v[138:139]
	v_lshl_add_u64 v[138:139], v[146:147], 1, v[138:139]
	v_cvt_pk_bf16_f32 v130, v142, v143
	v_cvt_pk_bf16_f32 v131, v140, v141
	v_cvt_pk_bf16_f32 v132, v148, v149
	v_cvt_pk_bf16_f32 v133, v144, v145
	global_store_dwordx4 v[138:139], v[130:133], off sc1
	s_and_b64 vcc, exec, s[4:5]
	s_nop 0
	v_pk_fma_f32 v[130:131], v[136:137], s[34:35], v[104:105] op_sel_hi:[1,0,1]
	v_pk_fma_f32 v[132:133], v[134:135], s[34:35], v[102:103] op_sel_hi:[1,0,1]
	v_pk_fma_f32 v[134:135], v[154:155], s[34:35], v[100:101] op_sel_hi:[1,0,1]
	v_pk_fma_f32 v[136:137], v[152:153], s[34:35], v[98:99] op_sel_hi:[1,0,1]
	s_cbranch_vccnz .LBB0_214
	v_mul_f32_e32 v132, 0xbfb8aa3b, v132
	v_mul_f32_e32 v136, 0xbfb8aa3b, v136
	v_mul_f32_e32 v133, 0xbfb8aa3b, v133
	v_mul_f32_e32 v137, 0xbfb8aa3b, v137
	v_mul_f32_e32 v130, 0xbfb8aa3b, v130
	v_mul_f32_e32 v134, 0xbfb8aa3b, v134
	v_mul_f32_e32 v131, 0xbfb8aa3b, v131
	v_mul_f32_e32 v135, 0xbfb8aa3b, v135
	v_exp_f32_e32 v132, v132
	v_exp_f32_e32 v136, v136
	v_exp_f32_e32 v133, v133
	v_exp_f32_e32 v137, v137
	v_exp_f32_e32 v130, v130
	v_exp_f32_e32 v134, v134
	v_exp_f32_e32 v131, v131
	v_exp_f32_e32 v135, v135
	v_add_f32_e32 v132, 1.0, v132
	v_add_f32_e32 v136, 1.0, v136
	v_add_f32_e32 v133, 1.0, v133
	v_add_f32_e32 v137, 1.0, v137
	v_add_f32_e32 v130, 1.0, v130
	v_add_f32_e32 v134, 1.0, v134
	v_add_f32_e32 v131, 1.0, v131
	v_add_f32_e32 v135, 1.0, v135
	v_rcp_f32_e32 v132, v132
	v_rcp_f32_e32 v136, v136
	v_rcp_f32_e32 v133, v133
	v_rcp_f32_e32 v137, v137
	v_rcp_f32_e32 v130, v130
	v_rcp_f32_e32 v134, v134
	v_rcp_f32_e32 v131, v131
	v_rcp_f32_e32 v135, v135
.LBB0_214:
	v_cvt_f32_i32_e32 v127, v127
	v_cvt_f32_i32_e32 v126, v126
	v_cvt_f32_i32_e32 v129, v129
	v_cvt_f32_i32_e32 v128, v128
	v_cvt_f32_i32_e32 v141, v123
	v_cvt_f32_i32_e32 v140, v122
	v_cvt_f32_i32_e32 v143, v125
	v_cvt_f32_i32_e32 v142, v124
	v_cvt_pk_bf16_f32 v122, v132, v133
	v_cvt_pk_bf16_f32 v123, v130, v131
	v_cvt_pk_bf16_f32 v124, v136, v137
	v_cvt_pk_bf16_f32 v125, v134, v135
	global_store_dwordx4 v[138:139], v[122:125], off offset:256 sc1
	v_pk_fma_f32 v[126:127], v[126:127], s[34:35], v[118:119] op_sel_hi:[1,0,1]
	s_and_b64 vcc, exec, s[4:5]
	v_pk_fma_f32 v[124:125], v[128:129], s[34:35], v[120:121] op_sel_hi:[1,0,1]
	v_pk_fma_f32 v[128:129], v[142:143], s[34:35], v[108:109] op_sel_hi:[1,0,1]
	v_pk_fma_f32 v[130:131], v[140:141], s[34:35], v[106:107] op_sel_hi:[1,0,1]
	s_cbranch_vccnz .LBB0_216
	v_mul_f32_e32 v122, 0xbfb8aa3b, v126
	v_exp_f32_e32 v122, v122
	v_mul_f32_e32 v123, 0xbfb8aa3b, v130
	v_exp_f32_e32 v123, v123
	v_add_f32_e32 v122, 1.0, v122
	v_rcp_f32_e32 v126, v122
	v_mul_f32_e32 v122, 0xbfb8aa3b, v127
	v_add_f32_e32 v123, 1.0, v123
	v_exp_f32_e32 v122, v122
	v_mul_f32_e32 v127, 0xbfb8aa3b, v131
	v_exp_f32_e32 v131, v127
	v_rcp_f32_e32 v130, v123
	v_mul_f32_e32 v123, 0xbfb8aa3b, v124
	v_exp_f32_e32 v123, v123
	v_add_f32_e32 v122, 1.0, v122
	v_rcp_f32_e32 v127, v122
	v_add_f32_e32 v122, 1.0, v131
	v_mul_f32_e32 v124, 0xbfb8aa3b, v128
	v_exp_f32_e32 v128, v124
	v_rcp_f32_e32 v131, v122
	v_add_f32_e32 v122, 1.0, v123
	v_mul_f32_e32 v123, 0xbfb8aa3b, v125
	v_exp_f32_e32 v123, v123
	v_mul_f32_e32 v125, 0xbfb8aa3b, v129
	v_exp_f32_e32 v129, v125
	v_rcp_f32_e32 v124, v122
	v_add_f32_e32 v122, 1.0, v128
	v_rcp_f32_e32 v128, v122
	v_add_f32_e32 v122, 1.0, v123
	v_rcp_f32_e32 v125, v122
	v_add_f32_e32 v122, 1.0, v129
	v_rcp_f32_e32 v129, v122
.LBB0_216:
	v_or_b32_e32 v132, 16, v150
	v_mov_b64_e32 v[122:123], s[54:55]
	v_mad_i64_i32 v[122:123], s[26:27], v132, s72, v[122:123]
	v_cvt_f32_i32_e32 v115, v115
	v_cvt_f32_i32_e32 v114, v114
	v_cvt_f32_i32_e32 v117, v117
	v_cvt_f32_i32_e32 v116, v116
	v_cvt_f32_i32_e32 v133, v111
	v_cvt_f32_i32_e32 v132, v110
	v_cvt_f32_i32_e32 v135, v113
	v_cvt_f32_i32_e32 v134, v112
	v_lshl_add_u64 v[122:123], v[146:147], 1, v[122:123]
	v_cvt_pk_bf16_f32 v110, v126, v127
	v_cvt_pk_bf16_f32 v111, v124, v125
	v_cvt_pk_bf16_f32 v112, v130, v131
	v_cvt_pk_bf16_f32 v113, v128, v129
	global_store_dwordx4 v[122:123], v[110:113], off sc1
	s_and_b64 vcc, exec, s[4:5]
	s_nop 0
	v_pk_fma_f32 v[110:111], v[116:117], s[34:35], v[104:105] op_sel_hi:[1,0,1]
	v_pk_fma_f32 v[112:113], v[114:115], s[34:35], v[102:103] op_sel_hi:[1,0,1]
	v_pk_fma_f32 v[114:115], v[134:135], s[34:35], v[100:101] op_sel_hi:[1,0,1]
	v_pk_fma_f32 v[116:117], v[132:133], s[34:35], v[98:99] op_sel_hi:[1,0,1]
	s_cbranch_vccnz .LBB0_218
	v_mul_f32_e32 v112, 0xbfb8aa3b, v112
	v_mul_f32_e32 v116, 0xbfb8aa3b, v116
	v_mul_f32_e32 v113, 0xbfb8aa3b, v113
	v_mul_f32_e32 v117, 0xbfb8aa3b, v117
	v_mul_f32_e32 v110, 0xbfb8aa3b, v110
	v_mul_f32_e32 v114, 0xbfb8aa3b, v114
	v_mul_f32_e32 v111, 0xbfb8aa3b, v111
	v_mul_f32_e32 v115, 0xbfb8aa3b, v115
	v_exp_f32_e32 v112, v112
	v_exp_f32_e32 v116, v116
	v_exp_f32_e32 v113, v113
	v_exp_f32_e32 v117, v117
	v_exp_f32_e32 v110, v110
	v_exp_f32_e32 v114, v114
	v_exp_f32_e32 v111, v111
	v_exp_f32_e32 v115, v115
	v_add_f32_e32 v112, 1.0, v112
	v_add_f32_e32 v116, 1.0, v116
	v_add_f32_e32 v113, 1.0, v113
	v_add_f32_e32 v117, 1.0, v117
	v_add_f32_e32 v110, 1.0, v110
	v_add_f32_e32 v114, 1.0, v114
	v_add_f32_e32 v111, 1.0, v111
	v_add_f32_e32 v115, 1.0, v115
	v_rcp_f32_e32 v112, v112
	v_rcp_f32_e32 v116, v116
	v_rcp_f32_e32 v113, v113
	v_rcp_f32_e32 v117, v117
	v_rcp_f32_e32 v110, v110
	v_rcp_f32_e32 v114, v114
	v_rcp_f32_e32 v111, v111
	v_rcp_f32_e32 v115, v115
; __device__ __forceinline__ unsigned cvt_pk_bf16(float lo, float hi) { unsigned r; asm volatile("v_cvt_pk_bf16_f32 %0, %1, %2" : "=v"(r) : "v"(lo), "v"(hi)); return r; }
; __device__ __forceinline__ float sigm(float x) { return __builtin_amdgcn_rcpf(1.0f + __builtin_amdgcn_exp2f(-1.4426950408889634f * x)); }
;     __device__ __forceinline__ void operator()(const f32x4 (&acc)[2][2][4][2], const Unit& u, int wr, int wc, int fr, int fq) const {
;     ...
;             for (int m = 0; m < 4; ++m) { bf16_t* rowp = Z + (size_t)(row0 + ai * HALF + m * 16) * ZLD + col0;
; #pragma unroll
;                 for (int bj = 0; bj < 2; ++bj) { f32x4 v0 = acc[ai][bj][m][0] * scale + bv[bj][0], v1 = acc[ai][bj][m][1] * scale + bv[bj][1];
;                     if (gate) {
; #pragma unroll
;                         for (int j = 0; j < 4; ++j) { v0[j] = sigm(v0[j]); v1[j] = sigm(v1[j]); } }
;                     u32x4 w; w.x = cvt_pk_bf16(v0[0], v0[1]); w.y = cvt_pk_bf16(v0[2], v0[3]); w.z = cvt_pk_bf16(v1[0], v1[1]); w.w = cvt_pk_bf16(v1[2], v1[3]);
;                     *(u32x4*)(rowp + bj * HALF) = w; } }
.LBB0_218:
	v_cvt_f32_i32_e32 v95, v95
	v_cvt_f32_i32_e32 v94, v94
	v_cvt_f32_i32_e32 v97, v97
	v_cvt_f32_i32_e32 v96, v96
	v_cvt_f32_i32_e32 v125, v91
	v_cvt_f32_i32_e32 v124, v90
	v_cvt_f32_i32_e32 v127, v93
	v_cvt_f32_i32_e32 v126, v92
	v_cvt_pk_bf16_f32 v90, v112, v113
	v_cvt_pk_bf16_f32 v91, v110, v111
	v_cvt_pk_bf16_f32 v92, v116, v117
	v_cvt_pk_bf16_f32 v93, v114, v115
	global_store_dwordx4 v[122:123], v[90:93], off offset:256 sc1
	v_pk_fma_f32 v[94:95], v[94:95], s[34:35], v[118:119] op_sel_hi:[1,0,1]
	s_and_b64 vcc, exec, s[4:5]
	v_pk_fma_f32 v[92:93], v[96:97], s[34:35], v[120:121] op_sel_hi:[1,0,1]
	v_pk_fma_f32 v[96:97], v[126:127], s[34:35], v[108:109] op_sel_hi:[1,0,1]
	v_pk_fma_f32 v[110:111], v[124:125], s[34:35], v[106:107] op_sel_hi:[1,0,1]
	s_cbranch_vccnz .LBB0_220
	v_mul_f32_e32 v90, 0xbfb8aa3b, v94
	v_exp_f32_e32 v90, v90
	v_mul_f32_e32 v91, 0xbfb8aa3b, v110
	v_exp_f32_e32 v91, v91
	v_add_f32_e32 v90, 1.0, v90
	v_rcp_f32_e32 v94, v90
	v_mul_f32_e32 v90, 0xbfb8aa3b, v95
	v_add_f32_e32 v91, 1.0, v91
	v_exp_f32_e32 v90, v90
	v_mul_f32_e32 v95, 0xbfb8aa3b, v111
	v_exp_f32_e32 v111, v95
	v_rcp_f32_e32 v110, v91
	v_mul_f32_e32 v91, 0xbfb8aa3b, v92
	v_exp_f32_e32 v91, v91
	v_add_f32_e32 v90, 1.0, v90
	v_rcp_f32_e32 v95, v90
	v_add_f32_e32 v90, 1.0, v111
	v_mul_f32_e32 v92, 0xbfb8aa3b, v96
	v_exp_f32_e32 v96, v92
	v_rcp_f32_e32 v111, v90
	v_add_f32_e32 v90, 1.0, v91
	v_mul_f32_e32 v91, 0xbfb8aa3b, v93
	v_exp_f32_e32 v91, v91
	v_mul_f32_e32 v93, 0xbfb8aa3b, v97
	v_exp_f32_e32 v97, v93
	v_rcp_f32_e32 v92, v90
	v_add_f32_e32 v90, 1.0, v96
	v_rcp_f32_e32 v96, v90
	v_add_f32_e32 v90, 1.0, v91
	v_rcp_f32_e32 v93, v90
	v_add_f32_e32 v90, 1.0, v97
	v_rcp_f32_e32 v97, v90
.LBB0_220:
	v_or_b32_e32 v112, 32, v150
	v_mov_b64_e32 v[90:91], s[54:55]
	v_mad_i64_i32 v[90:91], s[26:27], v112, s72, v[90:91]
	v_cvt_f32_i32_e32 v87, v87
	v_cvt_f32_i32_e32 v86, v86
	v_cvt_f32_i32_e32 v89, v89
	v_cvt_f32_i32_e32 v88, v88
	v_cvt_f32_i32_e32 v113, v83
	v_cvt_f32_i32_e32 v112, v82
	v_cvt_f32_i32_e32 v115, v85
	v_cvt_f32_i32_e32 v114, v84
	v_lshl_add_u64 v[90:91], v[146:147], 1, v[90:91]
	v_cvt_pk_bf16_f32 v82, v94, v95
	v_cvt_pk_bf16_f32 v83, v92, v93
	v_cvt_pk_bf16_f32 v84, v110, v111
	v_cvt_pk_bf16_f32 v85, v96, v97
	global_store_dwordx4 v[90:91], v[82:85], off sc1
	s_and_b64 vcc, exec, s[4:5]
	s_nop 0
	v_pk_fma_f32 v[82:83], v[88:89], s[34:35], v[104:105] op_sel_hi:[1,0,1]
	v_pk_fma_f32 v[84:85], v[86:87], s[34:35], v[102:103] op_sel_hi:[1,0,1]
	v_pk_fma_f32 v[86:87], v[114:115], s[34:35], v[100:101] op_sel_hi:[1,0,1]
	v_pk_fma_f32 v[88:89], v[112:113], s[34:35], v[98:99] op_sel_hi:[1,0,1]
	s_cbranch_vccnz .LBB0_222
	v_mul_f32_e32 v84, 0xbfb8aa3b, v84
	v_mul_f32_e32 v88, 0xbfb8aa3b, v88
	v_mul_f32_e32 v85, 0xbfb8aa3b, v85
	v_mul_f32_e32 v89, 0xbfb8aa3b, v89
	v_mul_f32_e32 v82, 0xbfb8aa3b, v82
	v_mul_f32_e32 v86, 0xbfb8aa3b, v86
	v_mul_f32_e32 v83, 0xbfb8aa3b, v83
	v_mul_f32_e32 v87, 0xbfb8aa3b, v87
	v_exp_f32_e32 v84, v84
	v_exp_f32_e32 v88, v88
	v_exp_f32_e32 v85, v85
	v_exp_f32_e32 v89, v89
	v_exp_f32_e32 v82, v82
	v_exp_f32_e32 v86, v86
	v_exp_f32_e32 v83, v83
	v_exp_f32_e32 v87, v87
	v_add_f32_e32 v84, 1.0, v84
	v_add_f32_e32 v88, 1.0, v88
	v_add_f32_e32 v85, 1.0, v85
	v_add_f32_e32 v89, 1.0, v89
	v_add_f32_e32 v82, 1.0, v82
	v_add_f32_e32 v86, 1.0, v86
	v_add_f32_e32 v83, 1.0, v83
	v_add_f32_e32 v87, 1.0, v87
	v_rcp_f32_e32 v84, v84
	v_rcp_f32_e32 v88, v88
	v_rcp_f32_e32 v85, v85
	v_rcp_f32_e32 v89, v89
	v_rcp_f32_e32 v82, v82
	v_rcp_f32_e32 v86, v86
	v_rcp_f32_e32 v83, v83
	v_rcp_f32_e32 v87, v87
.LBB0_222:
	v_cvt_f32_i32_e32 v79, v79
	v_cvt_f32_i32_e32 v78, v78
	v_cvt_f32_i32_e32 v81, v81
	v_cvt_f32_i32_e32 v80, v80
	v_cvt_f32_i32_e32 v93, v75
	v_cvt_f32_i32_e32 v92, v74
	v_cvt_f32_i32_e32 v95, v77
	v_cvt_f32_i32_e32 v94, v76
	v_cvt_pk_bf16_f32 v74, v84, v85
	v_cvt_pk_bf16_f32 v75, v82, v83
	v_cvt_pk_bf16_f32 v76, v88, v89
	v_cvt_pk_bf16_f32 v77, v86, v87
	global_store_dwordx4 v[90:91], v[74:77], off offset:256 sc1
	v_pk_fma_f32 v[78:79], v[78:79], s[34:35], v[118:119] op_sel_hi:[1,0,1]
	s_and_b64 vcc, exec, s[4:5]
	v_pk_fma_f32 v[76:77], v[80:81], s[34:35], v[120:121] op_sel_hi:[1,0,1]
	v_pk_fma_f32 v[80:81], v[94:95], s[34:35], v[108:109] op_sel_hi:[1,0,1]
	v_pk_fma_f32 v[82:83], v[92:93], s[34:35], v[106:107] op_sel_hi:[1,0,1]
	s_cbranch_vccnz .LBB0_224
	v_mul_f32_e32 v74, 0xbfb8aa3b, v78
	v_exp_f32_e32 v74, v74
	v_mul_f32_e32 v75, 0xbfb8aa3b, v82
	v_exp_f32_e32 v75, v75
	v_add_f32_e32 v74, 1.0, v74
	v_rcp_f32_e32 v78, v74
	v_mul_f32_e32 v74, 0xbfb8aa3b, v79
	v_add_f32_e32 v75, 1.0, v75
	v_exp_f32_e32 v74, v74
	v_mul_f32_e32 v79, 0xbfb8aa3b, v83
	v_exp_f32_e32 v83, v79
	v_rcp_f32_e32 v82, v75
	v_mul_f32_e32 v75, 0xbfb8aa3b, v76
	v_exp_f32_e32 v75, v75
	v_add_f32_e32 v74, 1.0, v74
	v_rcp_f32_e32 v79, v74
	v_add_f32_e32 v74, 1.0, v83
	v_mul_f32_e32 v76, 0xbfb8aa3b, v80
	v_exp_f32_e32 v80, v76
	v_rcp_f32_e32 v83, v74
	v_add_f32_e32 v74, 1.0, v75
	v_mul_f32_e32 v75, 0xbfb8aa3b, v77
	v_exp_f32_e32 v75, v75
	v_mul_f32_e32 v77, 0xbfb8aa3b, v81
	v_exp_f32_e32 v81, v77
	v_rcp_f32_e32 v76, v74
	v_add_f32_e32 v74, 1.0, v80
	v_rcp_f32_e32 v80, v74
	v_add_f32_e32 v74, 1.0, v75
	v_rcp_f32_e32 v77, v74
	v_add_f32_e32 v74, 1.0, v81
	v_rcp_f32_e32 v81, v74
; __device__ __forceinline__ unsigned cvt_pk_bf16(float lo, float hi) { unsigned r; asm volatile("v_cvt_pk_bf16_f32 %0, %1, %2" : "=v"(r) : "v"(lo), "v"(hi)); return r; }
; __device__ __forceinline__ float sigm(float x) { return __builtin_amdgcn_rcpf(1.0f + __builtin_amdgcn_exp2f(-1.4426950408889634f * x)); }
;     __device__ __forceinline__ void operator()(const f32x4 (&acc)[2][2][4][2], const Unit& u, int wr, int wc, int fr, int fq) const {
;     ...
;             for (int m = 0; m < 4; ++m) { bf16_t* rowp = Z + (size_t)(row0 + ai * HALF + m * 16) * ZLD + col0;
; #pragma unroll
;                 for (int bj = 0; bj < 2; ++bj) { f32x4 v0 = acc[ai][bj][m][0] * scale + bv[bj][0], v1 = acc[ai][bj][m][1] * scale + bv[bj][1];
;                     if (gate) {
; #pragma unroll
;                         for (int j = 0; j < 4; ++j) { v0[j] = sigm(v0[j]); v1[j] = sigm(v1[j]); } }
;                     u32x4 w; w.x = cvt_pk_bf16(v0[0], v0[1]); w.y = cvt_pk_bf16(v0[2], v0[3]); w.z = cvt_pk_bf16(v1[0], v1[1]); w.w = cvt_pk_bf16(v1[2], v1[3]);
;                     *(u32x4*)(rowp + bj * HALF) = w; } }
.LBB0_224:
	v_or_b32_e32 v84, 48, v150
	v_mov_b64_e32 v[74:75], s[54:55]
	v_mad_i64_i32 v[74:75], s[26:27], v84, s72, v[74:75]
	v_cvt_f32_i32_e32 v71, v71
	v_cvt_f32_i32_e32 v70, v70
	v_cvt_f32_i32_e32 v73, v73
	v_cvt_f32_i32_e32 v72, v72
	v_cvt_f32_i32_e32 v85, v67
	v_cvt_f32_i32_e32 v84, v66
	v_cvt_f32_i32_e32 v87, v69
	v_cvt_f32_i32_e32 v86, v68
	v_lshl_add_u64 v[74:75], v[146:147], 1, v[74:75]
	v_cvt_pk_bf16_f32 v66, v78, v79
	v_cvt_pk_bf16_f32 v67, v76, v77
	v_cvt_pk_bf16_f32 v68, v82, v83
	v_cvt_pk_bf16_f32 v69, v80, v81
	global_store_dwordx4 v[74:75], v[66:69], off sc1
	s_and_b64 vcc, exec, s[4:5]
	s_nop 0
	v_pk_fma_f32 v[66:67], v[72:73], s[34:35], v[104:105] op_sel_hi:[1,0,1]
	v_pk_fma_f32 v[68:69], v[70:71], s[34:35], v[102:103] op_sel_hi:[1,0,1]
	v_pk_fma_f32 v[70:71], v[86:87], s[34:35], v[100:101] op_sel_hi:[1,0,1]
	v_pk_fma_f32 v[72:73], v[84:85], s[34:35], v[98:99] op_sel_hi:[1,0,1]
	s_cbranch_vccnz .LBB0_226
	v_mul_f32_e32 v68, 0xbfb8aa3b, v68
	v_mul_f32_e32 v72, 0xbfb8aa3b, v72
	v_mul_f32_e32 v69, 0xbfb8aa3b, v69
	v_mul_f32_e32 v73, 0xbfb8aa3b, v73
	v_mul_f32_e32 v66, 0xbfb8aa3b, v66
	v_mul_f32_e32 v70, 0xbfb8aa3b, v70
	v_mul_f32_e32 v67, 0xbfb8aa3b, v67
	v_mul_f32_e32 v71, 0xbfb8aa3b, v71
	v_exp_f32_e32 v68, v68
	v_exp_f32_e32 v72, v72
	v_exp_f32_e32 v69, v69
	v_exp_f32_e32 v73, v73
	v_exp_f32_e32 v66, v66
	v_exp_f32_e32 v70, v70
	v_exp_f32_e32 v67, v67
	v_exp_f32_e32 v71, v71
	v_add_f32_e32 v68, 1.0, v68
	v_add_f32_e32 v72, 1.0, v72
	v_add_f32_e32 v69, 1.0, v69
	v_add_f32_e32 v73, 1.0, v73
	v_add_f32_e32 v66, 1.0, v66
	v_add_f32_e32 v70, 1.0, v70
	v_add_f32_e32 v67, 1.0, v67
	v_add_f32_e32 v71, 1.0, v71
	v_rcp_f32_e32 v68, v68
	v_rcp_f32_e32 v72, v72
	v_rcp_f32_e32 v69, v69
	v_rcp_f32_e32 v73, v73
	v_rcp_f32_e32 v66, v66
	v_rcp_f32_e32 v70, v70
	v_rcp_f32_e32 v67, v67
	v_rcp_f32_e32 v71, v71
.LBB0_226:
	v_cvt_f32_i32_e32 v63, v63
	v_cvt_f32_i32_e32 v62, v62
	v_cvt_f32_i32_e32 v65, v65
	v_cvt_f32_i32_e32 v64, v64
	v_cvt_f32_i32_e32 v77, v59
	v_cvt_f32_i32_e32 v76, v58
	v_cvt_f32_i32_e32 v79, v61
	v_cvt_f32_i32_e32 v78, v60
	v_cvt_pk_bf16_f32 v58, v68, v69
	v_cvt_pk_bf16_f32 v59, v66, v67
	v_cvt_pk_bf16_f32 v60, v72, v73
	v_cvt_pk_bf16_f32 v61, v70, v71
	global_store_dwordx4 v[74:75], v[58:61], off offset:256 sc1
	v_pk_fma_f32 v[62:63], v[62:63], s[34:35], v[118:119] op_sel_hi:[1,0,1]
	s_and_b64 vcc, exec, s[4:5]
	v_pk_fma_f32 v[60:61], v[64:65], s[34:35], v[120:121] op_sel_hi:[1,0,1]
	v_pk_fma_f32 v[64:65], v[78:79], s[34:35], v[108:109] op_sel_hi:[1,0,1]
	v_pk_fma_f32 v[66:67], v[76:77], s[34:35], v[106:107] op_sel_hi:[1,0,1]
	s_cbranch_vccnz .LBB0_228
	v_mul_f32_e32 v58, 0xbfb8aa3b, v62
	v_exp_f32_e32 v58, v58
	v_mul_f32_e32 v59, 0xbfb8aa3b, v66
	v_exp_f32_e32 v59, v59
	v_add_f32_e32 v58, 1.0, v58
	v_rcp_f32_e32 v62, v58
	v_mul_f32_e32 v58, 0xbfb8aa3b, v63
	v_add_f32_e32 v59, 1.0, v59
	v_exp_f32_e32 v58, v58
	v_mul_f32_e32 v63, 0xbfb8aa3b, v67
	v_exp_f32_e32 v67, v63
	v_rcp_f32_e32 v66, v59
	v_mul_f32_e32 v59, 0xbfb8aa3b, v60
	v_exp_f32_e32 v59, v59
	v_add_f32_e32 v58, 1.0, v58
	v_rcp_f32_e32 v63, v58
	v_add_f32_e32 v58, 1.0, v67
	v_mul_f32_e32 v60, 0xbfb8aa3b, v64
	v_exp_f32_e32 v64, v60
	v_rcp_f32_e32 v67, v58
	v_add_f32_e32 v58, 1.0, v59
	v_mul_f32_e32 v59, 0xbfb8aa3b, v61
	v_exp_f32_e32 v59, v59
	v_mul_f32_e32 v61, 0xbfb8aa3b, v65
	v_exp_f32_e32 v65, v61
	v_rcp_f32_e32 v60, v58
	v_add_f32_e32 v58, 1.0, v64
	v_rcp_f32_e32 v64, v58
	v_add_f32_e32 v58, 1.0, v59
	v_rcp_f32_e32 v61, v58
	v_add_f32_e32 v58, 1.0, v65
	v_rcp_f32_e32 v65, v58
.LBB0_228:
	v_add_u32_e32 v68, 0x80, v150
	v_mov_b64_e32 v[58:59], s[54:55]
	v_mad_i64_i32 v[58:59], s[26:27], v68, s72, v[58:59]
	v_cvt_f32_i32_e32 v55, v55
	v_cvt_f32_i32_e32 v54, v54
	v_cvt_f32_i32_e32 v57, v57
	v_cvt_f32_i32_e32 v56, v56
	v_cvt_f32_i32_e32 v69, v51
	v_cvt_f32_i32_e32 v68, v50
	v_cvt_f32_i32_e32 v71, v53
	v_cvt_f32_i32_e32 v70, v52
	v_lshl_add_u64 v[58:59], v[146:147], 1, v[58:59]
	v_cvt_pk_bf16_f32 v50, v62, v63
	v_cvt_pk_bf16_f32 v51, v60, v61
	v_cvt_pk_bf16_f32 v52, v66, v67
	v_cvt_pk_bf16_f32 v53, v64, v65
	global_store_dwordx4 v[58:59], v[50:53], off sc1
	s_and_b64 vcc, exec, s[4:5]
	s_nop 0
	v_pk_fma_f32 v[50:51], v[56:57], s[34:35], v[104:105] op_sel_hi:[1,0,1]
	v_pk_fma_f32 v[52:53], v[54:55], s[34:35], v[102:103] op_sel_hi:[1,0,1]
	v_pk_fma_f32 v[54:55], v[70:71], s[34:35], v[100:101] op_sel_hi:[1,0,1]
	v_pk_fma_f32 v[56:57], v[68:69], s[34:35], v[98:99] op_sel_hi:[1,0,1]
	s_cbranch_vccnz .LBB0_230
	v_mul_f32_e32 v52, 0xbfb8aa3b, v52
	v_mul_f32_e32 v56, 0xbfb8aa3b, v56
	v_mul_f32_e32 v53, 0xbfb8aa3b, v53
	v_mul_f32_e32 v57, 0xbfb8aa3b, v57
	v_mul_f32_e32 v50, 0xbfb8aa3b, v50
	v_mul_f32_e32 v54, 0xbfb8aa3b, v54
	v_mul_f32_e32 v51, 0xbfb8aa3b, v51
	v_mul_f32_e32 v55, 0xbfb8aa3b, v55
	v_exp_f32_e32 v52, v52
	v_exp_f32_e32 v56, v56
	v_exp_f32_e32 v53, v53
	v_exp_f32_e32 v57, v57
	v_exp_f32_e32 v50, v50
	v_exp_f32_e32 v54, v54
	v_exp_f32_e32 v51, v51
	v_exp_f32_e32 v55, v55
	v_add_f32_e32 v52, 1.0, v52
	v_add_f32_e32 v56, 1.0, v56
	v_add_f32_e32 v53, 1.0, v53
	v_add_f32_e32 v57, 1.0, v57
	v_add_f32_e32 v50, 1.0, v50
	v_add_f32_e32 v54, 1.0, v54
	v_add_f32_e32 v51, 1.0, v51
	v_add_f32_e32 v55, 1.0, v55
	v_rcp_f32_e32 v52, v52
	v_rcp_f32_e32 v56, v56
	v_rcp_f32_e32 v53, v53
	v_rcp_f32_e32 v57, v57
	v_rcp_f32_e32 v50, v50
	v_rcp_f32_e32 v54, v54
	v_rcp_f32_e32 v51, v51
	v_rcp_f32_e32 v55, v55
; __device__ __forceinline__ unsigned cvt_pk_bf16(float lo, float hi) { unsigned r; asm volatile("v_cvt_pk_bf16_f32 %0, %1, %2" : "=v"(r) : "v"(lo), "v"(hi)); return r; }
; __device__ __forceinline__ float sigm(float x) { return __builtin_amdgcn_rcpf(1.0f + __builtin_amdgcn_exp2f(-1.4426950408889634f * x)); }
;     __device__ __forceinline__ void operator()(const f32x4 (&acc)[2][2][4][2], const Unit& u, int wr, int wc, int fr, int fq) const {
;     ...
;             for (int m = 0; m < 4; ++m) { bf16_t* rowp = Z + (size_t)(row0 + ai * HALF + m * 16) * ZLD + col0;
; #pragma unroll
;                 for (int bj = 0; bj < 2; ++bj) { f32x4 v0 = acc[ai][bj][m][0] * scale + bv[bj][0], v1 = acc[ai][bj][m][1] * scale + bv[bj][1];
;                     if (gate) {
; #pragma unroll
;                         for (int j = 0; j < 4; ++j) { v0[j] = sigm(v0[j]); v1[j] = sigm(v1[j]); } }
;                     u32x4 w; w.x = cvt_pk_bf16(v0[0], v0[1]); w.y = cvt_pk_bf16(v0[2], v0[3]); w.z = cvt_pk_bf16(v1[0], v1[1]); w.w = cvt_pk_bf16(v1[2], v1[3]);
;                     *(u32x4*)(rowp + bj * HALF) = w; } }
.LBB0_230:
	v_cvt_f32_i32_e32 v47, v47
	v_cvt_f32_i32_e32 v46, v46
	v_cvt_f32_i32_e32 v49, v49
	v_cvt_f32_i32_e32 v48, v48
	v_cvt_f32_i32_e32 v61, v43
	v_cvt_f32_i32_e32 v60, v42
	v_cvt_f32_i32_e32 v63, v45
	v_cvt_f32_i32_e32 v62, v44
	v_cvt_pk_bf16_f32 v42, v52, v53
	v_cvt_pk_bf16_f32 v43, v50, v51
	v_cvt_pk_bf16_f32 v44, v56, v57
	v_cvt_pk_bf16_f32 v45, v54, v55
	global_store_dwordx4 v[58:59], v[42:45], off offset:256 sc1
	v_pk_fma_f32 v[46:47], v[46:47], s[34:35], v[118:119] op_sel_hi:[1,0,1]
	s_and_b64 vcc, exec, s[4:5]
	v_pk_fma_f32 v[44:45], v[48:49], s[34:35], v[120:121] op_sel_hi:[1,0,1]
	v_pk_fma_f32 v[48:49], v[62:63], s[34:35], v[108:109] op_sel_hi:[1,0,1]
	v_pk_fma_f32 v[50:51], v[60:61], s[34:35], v[106:107] op_sel_hi:[1,0,1]
	s_cbranch_vccnz .LBB0_232
	v_mul_f32_e32 v42, 0xbfb8aa3b, v46
	v_exp_f32_e32 v42, v42
	v_mul_f32_e32 v43, 0xbfb8aa3b, v50
	v_exp_f32_e32 v43, v43
	v_add_f32_e32 v42, 1.0, v42
	v_rcp_f32_e32 v46, v42
	v_mul_f32_e32 v42, 0xbfb8aa3b, v47
	v_add_f32_e32 v43, 1.0, v43
	v_exp_f32_e32 v42, v42
	v_mul_f32_e32 v47, 0xbfb8aa3b, v51
	v_exp_f32_e32 v51, v47
	v_rcp_f32_e32 v50, v43
	v_mul_f32_e32 v43, 0xbfb8aa3b, v44
	v_exp_f32_e32 v43, v43
	v_add_f32_e32 v42, 1.0, v42
	v_rcp_f32_e32 v47, v42
	v_add_f32_e32 v42, 1.0, v51
	v_mul_f32_e32 v44, 0xbfb8aa3b, v48
	v_exp_f32_e32 v48, v44
	v_rcp_f32_e32 v51, v42
	v_add_f32_e32 v42, 1.0, v43
	v_mul_f32_e32 v43, 0xbfb8aa3b, v45
	v_exp_f32_e32 v43, v43
	v_mul_f32_e32 v45, 0xbfb8aa3b, v49
	v_exp_f32_e32 v49, v45
	v_rcp_f32_e32 v44, v42
	v_add_f32_e32 v42, 1.0, v48
	v_rcp_f32_e32 v48, v42
	v_add_f32_e32 v42, 1.0, v43
	v_rcp_f32_e32 v45, v42
	v_add_f32_e32 v42, 1.0, v49
	v_rcp_f32_e32 v49, v42
.LBB0_232:
	v_add_u32_e32 v52, 0x90, v150
	v_mov_b64_e32 v[42:43], s[54:55]
	v_mad_i64_i32 v[42:43], s[26:27], v52, s72, v[42:43]
	v_cvt_f32_i32_e32 v39, v39
	v_cvt_f32_i32_e32 v38, v38
	v_cvt_f32_i32_e32 v41, v41
	v_cvt_f32_i32_e32 v40, v40
	v_cvt_f32_i32_e32 v53, v35
	v_cvt_f32_i32_e32 v52, v34
	v_cvt_f32_i32_e32 v55, v37
	v_cvt_f32_i32_e32 v54, v36
	v_lshl_add_u64 v[42:43], v[146:147], 1, v[42:43]
	v_cvt_pk_bf16_f32 v34, v46, v47
	v_cvt_pk_bf16_f32 v35, v44, v45
	v_cvt_pk_bf16_f32 v36, v50, v51
	v_cvt_pk_bf16_f32 v37, v48, v49
	global_store_dwordx4 v[42:43], v[34:37], off sc1
	s_and_b64 vcc, exec, s[4:5]
	s_nop 0
	v_pk_fma_f32 v[34:35], v[40:41], s[34:35], v[104:105] op_sel_hi:[1,0,1]
	v_pk_fma_f32 v[36:37], v[38:39], s[34:35], v[102:103] op_sel_hi:[1,0,1]
	v_pk_fma_f32 v[38:39], v[54:55], s[34:35], v[100:101] op_sel_hi:[1,0,1]
	v_pk_fma_f32 v[40:41], v[52:53], s[34:35], v[98:99] op_sel_hi:[1,0,1]
	s_cbranch_vccnz .LBB0_234
	v_mul_f32_e32 v36, 0xbfb8aa3b, v36
	v_mul_f32_e32 v40, 0xbfb8aa3b, v40
	v_mul_f32_e32 v37, 0xbfb8aa3b, v37
	v_mul_f32_e32 v41, 0xbfb8aa3b, v41
	v_mul_f32_e32 v34, 0xbfb8aa3b, v34
	v_mul_f32_e32 v38, 0xbfb8aa3b, v38
	v_mul_f32_e32 v35, 0xbfb8aa3b, v35
	v_mul_f32_e32 v39, 0xbfb8aa3b, v39
	v_exp_f32_e32 v36, v36
	v_exp_f32_e32 v40, v40
	v_exp_f32_e32 v37, v37
	v_exp_f32_e32 v41, v41
	v_exp_f32_e32 v34, v34
	v_exp_f32_e32 v38, v38
	v_exp_f32_e32 v35, v35
	v_exp_f32_e32 v39, v39
	v_add_f32_e32 v36, 1.0, v36
	v_add_f32_e32 v40, 1.0, v40
	v_add_f32_e32 v37, 1.0, v37
	v_add_f32_e32 v41, 1.0, v41
	v_add_f32_e32 v34, 1.0, v34
	v_add_f32_e32 v38, 1.0, v38
	v_add_f32_e32 v35, 1.0, v35
	v_add_f32_e32 v39, 1.0, v39
	v_rcp_f32_e32 v36, v36
	v_rcp_f32_e32 v40, v40
	v_rcp_f32_e32 v37, v37
	v_rcp_f32_e32 v41, v41
	v_rcp_f32_e32 v34, v34
	v_rcp_f32_e32 v38, v38
	v_rcp_f32_e32 v35, v35
	v_rcp_f32_e32 v39, v39
.LBB0_234:
	v_cvt_f32_i32_e32 v31, v31
	v_cvt_f32_i32_e32 v30, v30
	v_cvt_f32_i32_e32 v33, v33
	v_cvt_f32_i32_e32 v32, v32
	v_cvt_f32_i32_e32 v45, v27
	v_cvt_f32_i32_e32 v44, v26
	v_cvt_f32_i32_e32 v47, v29
	v_cvt_f32_i32_e32 v46, v28
	v_cvt_pk_bf16_f32 v26, v36, v37
	v_cvt_pk_bf16_f32 v27, v34, v35
	v_cvt_pk_bf16_f32 v28, v40, v41
	v_cvt_pk_bf16_f32 v29, v38, v39
	global_store_dwordx4 v[42:43], v[26:29], off offset:256 sc1
	v_pk_fma_f32 v[30:31], v[30:31], s[34:35], v[118:119] op_sel_hi:[1,0,1]
	s_and_b64 vcc, exec, s[4:5]
	v_pk_fma_f32 v[28:29], v[32:33], s[34:35], v[120:121] op_sel_hi:[1,0,1]
	v_pk_fma_f32 v[32:33], v[46:47], s[34:35], v[108:109] op_sel_hi:[1,0,1]
	v_pk_fma_f32 v[34:35], v[44:45], s[34:35], v[106:107] op_sel_hi:[1,0,1]
	s_cbranch_vccnz .LBB0_236
	v_mul_f32_e32 v26, 0xbfb8aa3b, v30
	v_exp_f32_e32 v26, v26
	v_mul_f32_e32 v27, 0xbfb8aa3b, v34
	v_exp_f32_e32 v27, v27
	v_add_f32_e32 v26, 1.0, v26
	v_rcp_f32_e32 v30, v26
	v_mul_f32_e32 v26, 0xbfb8aa3b, v31
	v_add_f32_e32 v27, 1.0, v27
	v_exp_f32_e32 v26, v26
	v_mul_f32_e32 v31, 0xbfb8aa3b, v35
	v_exp_f32_e32 v35, v31
	v_rcp_f32_e32 v34, v27
	v_mul_f32_e32 v27, 0xbfb8aa3b, v28
	v_exp_f32_e32 v27, v27
	v_add_f32_e32 v26, 1.0, v26
	v_rcp_f32_e32 v31, v26
	v_add_f32_e32 v26, 1.0, v35
	v_mul_f32_e32 v28, 0xbfb8aa3b, v32
	v_exp_f32_e32 v32, v28
	v_rcp_f32_e32 v35, v26
	v_add_f32_e32 v26, 1.0, v27
	v_mul_f32_e32 v27, 0xbfb8aa3b, v29
	v_exp_f32_e32 v27, v27
	v_mul_f32_e32 v29, 0xbfb8aa3b, v33
	v_exp_f32_e32 v33, v29
	v_rcp_f32_e32 v28, v26
	v_add_f32_e32 v26, 1.0, v32
	v_rcp_f32_e32 v32, v26
	v_add_f32_e32 v26, 1.0, v27
	v_rcp_f32_e32 v29, v26
	v_add_f32_e32 v26, 1.0, v33
	v_rcp_f32_e32 v33, v26
; __device__ __forceinline__ unsigned cvt_pk_bf16(float lo, float hi) { unsigned r; asm volatile("v_cvt_pk_bf16_f32 %0, %1, %2" : "=v"(r) : "v"(lo), "v"(hi)); return r; }
; __device__ __forceinline__ float sigm(float x) { return __builtin_amdgcn_rcpf(1.0f + __builtin_amdgcn_exp2f(-1.4426950408889634f * x)); }
;     __device__ __forceinline__ void operator()(const f32x4 (&acc)[2][2][4][2], const Unit& u, int wr, int wc, int fr, int fq) const {
;     ...
;             for (int m = 0; m < 4; ++m) { bf16_t* rowp = Z + (size_t)(row0 + ai * HALF + m * 16) * ZLD + col0;
; #pragma unroll
;                 for (int bj = 0; bj < 2; ++bj) { f32x4 v0 = acc[ai][bj][m][0] * scale + bv[bj][0], v1 = acc[ai][bj][m][1] * scale + bv[bj][1];
;                     if (gate) {
; #pragma unroll
;                         for (int j = 0; j < 4; ++j) { v0[j] = sigm(v0[j]); v1[j] = sigm(v1[j]); } }
;                     u32x4 w; w.x = cvt_pk_bf16(v0[0], v0[1]); w.y = cvt_pk_bf16(v0[2], v0[3]); w.z = cvt_pk_bf16(v1[0], v1[1]); w.w = cvt_pk_bf16(v1[2], v1[3]);
;                     *(u32x4*)(rowp + bj * HALF) = w; } }
.LBB0_236:
	v_add_u32_e32 v36, 0xa0, v150
	v_mov_b64_e32 v[26:27], s[54:55]
	v_mad_i64_i32 v[26:27], s[26:27], v36, s72, v[26:27]
	v_cvt_f32_i32_e32 v23, v23
	v_cvt_f32_i32_e32 v22, v22
	v_cvt_f32_i32_e32 v25, v25
	v_cvt_f32_i32_e32 v24, v24
	v_cvt_f32_i32_e32 v37, v19
	v_cvt_f32_i32_e32 v36, v18
	v_cvt_f32_i32_e32 v39, v21
	v_cvt_f32_i32_e32 v38, v20
	v_lshl_add_u64 v[26:27], v[146:147], 1, v[26:27]
	v_cvt_pk_bf16_f32 v18, v30, v31
	v_cvt_pk_bf16_f32 v19, v28, v29
	v_cvt_pk_bf16_f32 v20, v34, v35
	v_cvt_pk_bf16_f32 v21, v32, v33
	global_store_dwordx4 v[26:27], v[18:21], off sc1
	s_and_b64 vcc, exec, s[4:5]
	s_nop 0
	v_pk_fma_f32 v[18:19], v[24:25], s[34:35], v[104:105] op_sel_hi:[1,0,1]
	v_pk_fma_f32 v[20:21], v[22:23], s[34:35], v[102:103] op_sel_hi:[1,0,1]
	v_pk_fma_f32 v[22:23], v[38:39], s[34:35], v[100:101] op_sel_hi:[1,0,1]
	v_pk_fma_f32 v[24:25], v[36:37], s[34:35], v[98:99] op_sel_hi:[1,0,1]
	s_cbranch_vccnz .LBB0_238
	v_mul_f32_e32 v20, 0xbfb8aa3b, v20
	v_mul_f32_e32 v24, 0xbfb8aa3b, v24
	v_mul_f32_e32 v21, 0xbfb8aa3b, v21
	v_mul_f32_e32 v25, 0xbfb8aa3b, v25
	v_mul_f32_e32 v18, 0xbfb8aa3b, v18
	v_mul_f32_e32 v22, 0xbfb8aa3b, v22
	v_mul_f32_e32 v19, 0xbfb8aa3b, v19
	v_mul_f32_e32 v23, 0xbfb8aa3b, v23
	v_exp_f32_e32 v20, v20
	v_exp_f32_e32 v24, v24
	v_exp_f32_e32 v21, v21
	v_exp_f32_e32 v25, v25
	v_exp_f32_e32 v18, v18
	v_exp_f32_e32 v22, v22
	v_exp_f32_e32 v19, v19
	v_exp_f32_e32 v23, v23
	v_add_f32_e32 v20, 1.0, v20
	v_add_f32_e32 v24, 1.0, v24
	v_add_f32_e32 v21, 1.0, v21
	v_add_f32_e32 v25, 1.0, v25
	v_add_f32_e32 v18, 1.0, v18
	v_add_f32_e32 v22, 1.0, v22
	v_add_f32_e32 v19, 1.0, v19
	v_add_f32_e32 v23, 1.0, v23
	v_rcp_f32_e32 v20, v20
	v_rcp_f32_e32 v24, v24
	v_rcp_f32_e32 v21, v21
	v_rcp_f32_e32 v25, v25
	v_rcp_f32_e32 v18, v18
	v_rcp_f32_e32 v22, v22
	v_rcp_f32_e32 v19, v19
	v_rcp_f32_e32 v23, v23
.LBB0_238:
	v_cvt_f32_i32_e32 v15, v15
	v_cvt_f32_i32_e32 v14, v14
	v_cvt_f32_i32_e32 v17, v17
	v_cvt_f32_i32_e32 v16, v16
	v_cvt_f32_i32_e32 v29, v11
	v_cvt_f32_i32_e32 v28, v10
	v_cvt_f32_i32_e32 v31, v13
	v_cvt_f32_i32_e32 v30, v12
	v_cvt_pk_bf16_f32 v10, v20, v21
	v_cvt_pk_bf16_f32 v11, v18, v19
	v_cvt_pk_bf16_f32 v12, v24, v25
	v_cvt_pk_bf16_f32 v13, v22, v23
	global_store_dwordx4 v[26:27], v[10:13], off offset:256 sc1
	v_pk_fma_f32 v[14:15], v[14:15], s[34:35], v[118:119] op_sel_hi:[1,0,1]
	s_and_b64 vcc, exec, s[4:5]
	v_pk_fma_f32 v[12:13], v[16:17], s[34:35], v[120:121] op_sel_hi:[1,0,1]
	v_pk_fma_f32 v[16:17], v[30:31], s[34:35], v[108:109] op_sel_hi:[1,0,1]
	v_pk_fma_f32 v[18:19], v[28:29], s[34:35], v[106:107] op_sel_hi:[1,0,1]
	s_cbranch_vccnz .LBB0_240
	v_mul_f32_e32 v10, 0xbfb8aa3b, v14
	v_exp_f32_e32 v10, v10
	v_mul_f32_e32 v11, 0xbfb8aa3b, v18
	v_exp_f32_e32 v11, v11
	v_add_f32_e32 v10, 1.0, v10
	v_rcp_f32_e32 v14, v10
	v_mul_f32_e32 v10, 0xbfb8aa3b, v15
	v_add_f32_e32 v11, 1.0, v11
	v_exp_f32_e32 v10, v10
	v_mul_f32_e32 v15, 0xbfb8aa3b, v19
	v_exp_f32_e32 v19, v15
	v_rcp_f32_e32 v18, v11
	v_mul_f32_e32 v11, 0xbfb8aa3b, v12
	v_exp_f32_e32 v11, v11
	v_add_f32_e32 v10, 1.0, v10
	v_rcp_f32_e32 v15, v10
	v_add_f32_e32 v10, 1.0, v19
	v_mul_f32_e32 v12, 0xbfb8aa3b, v16
	v_exp_f32_e32 v16, v12
	v_rcp_f32_e32 v19, v10
	v_add_f32_e32 v10, 1.0, v11
	v_mul_f32_e32 v11, 0xbfb8aa3b, v13
	v_exp_f32_e32 v11, v11
	v_mul_f32_e32 v13, 0xbfb8aa3b, v17
	v_exp_f32_e32 v17, v13
	v_rcp_f32_e32 v12, v10
	v_add_f32_e32 v10, 1.0, v16
	v_rcp_f32_e32 v16, v10
	v_add_f32_e32 v10, 1.0, v11
	v_rcp_f32_e32 v13, v10
	v_add_f32_e32 v10, 1.0, v17
	v_rcp_f32_e32 v17, v10
.LBB0_240:
	v_add_u32_e32 v20, 0xb0, v150
	v_mov_b64_e32 v[10:11], s[54:55]
	v_mad_i64_i32 v[10:11], s[26:27], v20, s72, v[10:11]
	v_cvt_f32_i32_e32 v7, v7
	v_cvt_f32_i32_e32 v6, v6
	v_cvt_f32_i32_e32 v9, v9
	v_cvt_f32_i32_e32 v8, v8
	v_cvt_f32_i32_e32 v21, v3
	v_cvt_f32_i32_e32 v20, v2
	v_cvt_f32_i32_e32 v23, v5
	v_cvt_f32_i32_e32 v22, v4
	v_lshl_add_u64 v[10:11], v[146:147], 1, v[10:11]
	v_cvt_pk_bf16_f32 v2, v14, v15
	v_cvt_pk_bf16_f32 v3, v12, v13
	v_cvt_pk_bf16_f32 v4, v18, v19
	v_cvt_pk_bf16_f32 v5, v16, v17
	global_store_dwordx4 v[10:11], v[2:5], off sc1
	s_and_b64 vcc, exec, s[4:5]
	s_nop 0
	v_pk_fma_f32 v[2:3], v[8:9], s[34:35], v[104:105] op_sel_hi:[1,0,1]
	v_pk_fma_f32 v[4:5], v[6:7], s[34:35], v[102:103] op_sel_hi:[1,0,1]
	v_pk_fma_f32 v[6:7], v[22:23], s[34:35], v[100:101] op_sel_hi:[1,0,1]
	v_pk_fma_f32 v[8:9], v[20:21], s[34:35], v[98:99] op_sel_hi:[1,0,1]
	s_cbranch_vccnz .LBB0_242
	v_mul_f32_e32 v4, 0xbfb8aa3b, v4
	v_mul_f32_e32 v8, 0xbfb8aa3b, v8
	v_mul_f32_e32 v5, 0xbfb8aa3b, v5
	v_mul_f32_e32 v9, 0xbfb8aa3b, v9
	v_mul_f32_e32 v2, 0xbfb8aa3b, v2
	v_mul_f32_e32 v6, 0xbfb8aa3b, v6
	v_mul_f32_e32 v3, 0xbfb8aa3b, v3
	v_mul_f32_e32 v7, 0xbfb8aa3b, v7
	v_exp_f32_e32 v4, v4
	v_exp_f32_e32 v8, v8
	v_exp_f32_e32 v5, v5
	v_exp_f32_e32 v9, v9
	v_exp_f32_e32 v2, v2
	v_exp_f32_e32 v6, v6
	v_exp_f32_e32 v3, v3
	v_exp_f32_e32 v7, v7
	v_add_f32_e32 v4, 1.0, v4
	v_add_f32_e32 v8, 1.0, v8
	v_add_f32_e32 v5, 1.0, v5
	v_add_f32_e32 v9, 1.0, v9
	v_add_f32_e32 v2, 1.0, v2
	v_add_f32_e32 v6, 1.0, v6
	v_add_f32_e32 v3, 1.0, v3
	v_add_f32_e32 v7, 1.0, v7
	v_rcp_f32_e32 v4, v4
	v_rcp_f32_e32 v8, v8
	v_rcp_f32_e32 v5, v5
	v_rcp_f32_e32 v9, v9
	v_rcp_f32_e32 v2, v2
	v_rcp_f32_e32 v6, v6
	v_rcp_f32_e32 v3, v3
	v_rcp_f32_e32 v7, v7
.LBB0_242:
	s_andn2_b64 vcc, exec, s[0:1]
	s_mov_b64 s[0:1], -1
	v_cvt_pk_bf16_f32 v12, v4, v5
	v_cvt_pk_bf16_f32 v13, v2, v3
	v_cvt_pk_bf16_f32 v14, v8, v9
	v_cvt_pk_bf16_f32 v15, v6, v7
	global_store_dwordx4 v[10:11], v[12:15], off offset:256 sc1
	s_cbranch_vccnz .LBB0_246
	s_andn2_b64 vcc, exec, s[28:29]
	s_cbranch_vccnz .LBB0_245
	s_barrier
